# LDS-DMA: 11 of 16 Wv fragments per wave staged into unused LDS during the streaming loop (tile 8) and read back with ds_read_b128 in the epilogue; on top of early-3-tiles prologue + ring + static prio
# speedup vs baseline: 1.0118x; 1.0118x over previous
.LBB1_8:
	s_or_b64 exec, exec, s[2:3]
	s_nop 4
	v_lshlrev_b32_e32 v156, 11, v197
	v_lshl_or_b32 v156, v184, 2, v156
	s_waitcnt lgkmcnt(0)
	s_barrier
	ds_read_b128 v[10:13], v156 offset:16640
	ds_read_b128 v[6:9], v156 offset:17664
	v_and_b32_e32 v2, 8, v0
	v_cmp_eq_u32_e64 s[4:5], 0, v2
	v_and_b32_e32 v2, 4, v0
	s_load_dwordx2 s[18:19], s[0:1], 0x70
	v_cmp_eq_u32_e64 s[2:3], 0, v2
	v_and_b32_e32 v2, 3, v0
	s_movk_i32 s0, 0x320
	v_cmp_eq_u32_e32 vcc, 0, v2
	v_mad_i64_i32 v[2:3], s[0:1], v104, s0, 0
	v_or_b32_e32 v2, v2, v108
	v_bfe_u32 v109, v0, 2, 1
	v_lshl_add_u64 v[2:3], s[16:17], 0, v[2:3]
	v_lshl_add_u64 v[118:119], v[2:3], 0, 64
	v_lshl_add_u64 v[118:119], v[118:119], 0, 32
	v_mul_u32_u24_e32 v2, 0x320, v109
	s_movk_i32 s0, 0x640
	v_mad_u32_u24 v2, v197, s0, v2
	v_and_b32_e32 v199, 31, v0
	v_or_b32_e32 v2, v2, v108
	v_lshlrev_b32_e32 v186, 4, v199
	v_mov_b32_e32 v187, 0
	v_add_u32_e32 v114, 0x8200, v2
	v_lshl_add_u64 v[2:3], v[78:79], 0, v[186:187]
	v_lshl_add_u64 v[2:3], v[102:103], 0, v[2:3]
	s_mov_b64 s[0:1], 0x3000
	v_add_u32_e32 v201, 0xe500, v105
	v_lshl_add_u64 v[116:117], v[2:3], 0, s[0:1]
	v_mov_b32_e32 v104, 0xff800000
	v_mov_b32_e32 v113, 0xd01502f9
	s_mov_b64 s[16:17], 0x1000
	v_mov_b32_e32 v96, 0
	v_mov_b32_e32 v97, 0
	v_mov_b32_e32 v98, 0
	v_mov_b32_e32 v99, 0
	v_mov_b32_e32 v100, 0
	v_mov_b32_e32 v101, 0
	v_mov_b32_e32 v102, 0
	v_mov_b32_e32 v103, 0
	v_mov_b32_e32 v105, 0
	s_mov_b32 s30, 0
	global_load_dword v205, v[118:119], off nt
	global_load_dwordx4 v[138:141], v[116:117], off nt
	global_load_dwordx4 v[146:149], v[116:117], off offset:512 nt
	global_load_dwordx4 v[152:155], v[116:117], off offset:1024 nt
	global_load_dwordx4 v[156:159], v[116:117], off offset:1536 nt
	global_load_dwordx4 v[160:163], v[116:117], off offset:2048 nt
	global_load_dwordx4 v[164:167], v[116:117], off offset:2560 nt
	global_load_dwordx4 v[168:171], v[116:117], off offset:3072 nt
	global_load_dwordx4 v[172:175], v[116:117], off offset:3584 nt
	v_lshl_add_u64 v[116:117], v[116:117], 0, s[16:17]
	v_lshl_add_u64 v[118:119], v[118:119], 0, 32
	v_readfirstlane_b32 s32, v197
	s_nop 3
	s_mul_i32 s33, s32, 11264
	s_add_u32 s33, s33, 71424
	s_cmp_lt_u32 s32, 4
	s_cbranch_scc1 .Lring_prio_done
	s_setprio 1

.Lring_go_0:
	v_mul_f32_e32 v74, v10, v70
	v_mul_f32_e32 v75, v6, v70
	v_mul_f32_e32 v76, v10, v66
	v_mul_f32_e32 v77, v6, v66
	v_mul_f32_e32 v78, v10, v62
	v_mul_f32_e32 v79, v6, v62
	v_mul_f32_e32 v80, v10, v58
	v_mul_f32_e32 v81, v6, v58
	v_mul_f32_e32 v82, v10, v54
	v_mul_f32_e32 v83, v6, v54
	v_mul_f32_e32 v84, v10, v46
	v_mul_f32_e32 v85, v6, v46
	v_mul_f32_e32 v86, v10, v34
	v_mul_f32_e32 v87, v6, v34
	v_mul_f32_e32 v88, v10, v14
	v_mul_f32_e32 v89, v6, v14
	v_fmac_f32_e32 v74, v71, v11
	v_fmac_f32_e32 v75, v71, v7
	v_fmac_f32_e32 v76, v67, v11
	v_fmac_f32_e32 v77, v67, v7
	v_fmac_f32_e32 v78, v63, v11
	v_fmac_f32_e32 v79, v63, v7
	v_fmac_f32_e32 v80, v59, v11
	v_fmac_f32_e32 v81, v59, v7
	v_fmac_f32_e32 v82, v55, v11
	v_fmac_f32_e32 v83, v55, v7
	v_fmac_f32_e32 v84, v47, v11
	v_fmac_f32_e32 v85, v47, v7
	v_fmac_f32_e32 v86, v35, v11
	v_fmac_f32_e32 v87, v35, v7
	v_fmac_f32_e32 v88, v15, v11
	v_fmac_f32_e32 v89, v15, v7
	v_fmac_f32_e32 v74, v72, v12
	v_fmac_f32_e32 v75, v72, v8
	v_fmac_f32_e32 v76, v68, v12
	v_fmac_f32_e32 v77, v68, v8
	v_fmac_f32_e32 v78, v64, v12
	v_fmac_f32_e32 v79, v64, v8
	v_fmac_f32_e32 v80, v60, v12
	v_fmac_f32_e32 v81, v60, v8
	v_fmac_f32_e32 v82, v56, v12
	v_fmac_f32_e32 v83, v56, v8
	v_fmac_f32_e32 v84, v48, v12
	v_fmac_f32_e32 v85, v48, v8
	v_fmac_f32_e32 v86, v36, v12
	v_fmac_f32_e32 v87, v36, v8
	v_fmac_f32_e32 v88, v16, v12
	v_fmac_f32_e32 v89, v16, v8
	v_fmac_f32_e32 v74, v73, v13
	v_fmac_f32_e32 v75, v73, v9
	v_fmac_f32_e32 v76, v69, v13
	v_fmac_f32_e32 v77, v69, v9
	v_fmac_f32_e32 v78, v65, v13
	v_fmac_f32_e32 v79, v65, v9
	v_fmac_f32_e32 v80, v61, v13
	v_fmac_f32_e32 v81, v61, v9
	v_fmac_f32_e32 v82, v57, v13
	v_fmac_f32_e32 v83, v57, v9
	v_fmac_f32_e32 v84, v49, v13
	v_fmac_f32_e32 v85, v49, v9
	v_fmac_f32_e32 v86, v37, v13
	v_fmac_f32_e32 v87, v37, v9
	v_fmac_f32_e32 v88, v17, v13
	v_fmac_f32_e32 v89, v17, v9
	v_permlane32_swap_b32_e32 v74, v82
	v_permlane32_swap_b32_e32 v75, v83
	v_permlane32_swap_b32_e32 v76, v84
	v_permlane32_swap_b32_e32 v77, v85
	v_permlane32_swap_b32_e32 v78, v86
	v_permlane32_swap_b32_e32 v79, v87
	v_permlane32_swap_b32_e32 v80, v88
	v_permlane32_swap_b32_e32 v81, v89
	v_add_f32_e32 v74, v74, v82
	v_add_f32_e32 v75, v75, v83
	v_add_f32_e32 v76, v76, v84
	v_add_f32_e32 v77, v77, v85
	v_add_f32_e32 v78, v78, v86
	v_add_f32_e32 v79, v79, v87
	v_add_f32_e32 v80, v80, v88
	v_add_f32_e32 v81, v81, v89
	v_permlane16_swap_b32_e32 v74, v78
	v_permlane16_swap_b32_e32 v75, v79
	v_permlane16_swap_b32_e32 v76, v80
	v_permlane16_swap_b32_e32 v77, v81
	v_add_f32_e32 v74, v74, v78
	v_add_f32_e32 v75, v75, v79
	v_add_f32_e32 v76, v76, v80
	v_add_f32_e32 v77, v77, v81
	v_add_f32_dpp v74, v74, v74 row_ror:8 row_mask:0xf bank_mask:0xf bound_ctrl:1
	v_add_f32_dpp v76, v76, v76 row_ror:8 row_mask:0xf bank_mask:0xf bound_ctrl:1
	v_add_f32_dpp v75, v75, v75 row_ror:8 row_mask:0xf bank_mask:0xf bound_ctrl:1
	v_add_f32_dpp v77, v77, v77 row_ror:8 row_mask:0xf bank_mask:0xf bound_ctrl:1
	v_cndmask_b32_e64 v74, v76, v74, s[4:5]
	v_cndmask_b32_e64 v75, v77, v75, s[4:5]
	v_cmp_eq_u32_e64 s[0:1], 0, v107
	v_add_f32_dpp v74, v74, v74 row_half_mirror row_mask:0xf bank_mask:0xf bound_ctrl:1
	v_add_f32_dpp v75, v75, v75 row_half_mirror row_mask:0xf bank_mask:0xf bound_ctrl:1
	v_cndmask_b32_e64 v74, v75, v74, s[2:3]
	s_nop 1
	v_add_f32_dpp v74, v74, v74 quad_perm:[2,3,0,1] row_mask:0xf bank_mask:0xf bound_ctrl:1
	s_nop 1
	v_add_f32_dpp v74, v74, v74 quad_perm:[1,0,3,2] row_mask:0xf bank_mask:0xf bound_ctrl:1
	v_cndmask_b32_e64 v74, v113, v74, s[0:1]
	s_and_saveexec_b64 s[0:1], vcc
	ds_write_b32 v114, v74
	s_or_b64 exec, exec, s[0:1]
	v_mov_b32_dpp v90, v74 row_ror:8 row_mask:0xf bank_mask:0xf bound_ctrl:1
	v_add_u32_e32 v114, 32, v114
	v_max_f32_e32 v90, v74, v90
	v_mov_b32_e32 v91, v90
	s_nop 1
	v_permlane16_swap_b32_e32 v90, v91
	s_nop 0
	v_max_f32_e32 v90, v90, v91
	v_mov_b32_e32 v91, v90
	s_nop 1
	v_permlane32_swap_b32_e32 v90, v91
	s_nop 0
	v_max3_f32 v92, v104, v90, v91
	v_sub_f32_e32 v93, v104, v92
	v_sub_f32_e32 v94, v74, v92
	v_exp_f32_e32 v93, v93
	v_exp_f32_e32 v94, v94
	v_mov_b32_e32 v104, v92
	s_nop 1
	v_fma_f32 v105, v105, v93, v94
	s_nop 0
	v_readlane_b32 s34, v93, 0
	v_readlane_b32 s36, v93, 4
	v_readlane_b32 s38, v94, 0
	v_readlane_b32 s40, v94, 4
	v_readlane_b32 s42, v94, 8
	v_readlane_b32 s44, v94, 12
	v_readlane_b32 s46, v94, 16
	v_readlane_b32 s48, v94, 20
	v_readlane_b32 s50, v94, 24
	v_readlane_b32 s52, v94, 28
	v_readlane_b32 s54, v94, 32
	v_readlane_b32 s56, v94, 36
	v_readlane_b32 s58, v94, 40
	v_readlane_b32 s60, v94, 44
	v_readlane_b32 s62, v94, 48
	v_readlane_b32 s64, v94, 52
	v_readlane_b32 s66, v94, 56
	v_readlane_b32 s68, v94, 60
	s_nop 1
	v_pk_mul_f32 v[96:97], v[96:97], s[34:35] op_sel_hi:[1,0]
	v_pk_mul_f32 v[98:99], v[98:99], s[34:35] op_sel_hi:[1,0]
	v_pk_mul_f32 v[100:101], v[100:101], s[36:37] op_sel_hi:[1,0]
	v_pk_mul_f32 v[102:103], v[102:103], s[36:37] op_sel_hi:[1,0]
	v_pk_fma_f32 v[96:97], v[70:71], s[38:39], v[96:97] op_sel_hi:[1,0,1]
	v_pk_fma_f32 v[98:99], v[72:73], s[38:39], v[98:99] op_sel_hi:[1,0,1]
	v_pk_fma_f32 v[100:101], v[70:71], s[40:41], v[100:101] op_sel_hi:[1,0,1]
	v_pk_fma_f32 v[102:103], v[72:73], s[40:41], v[102:103] op_sel_hi:[1,0,1]
	v_pk_fma_f32 v[96:97], v[66:67], s[42:43], v[96:97] op_sel_hi:[1,0,1]
	v_pk_fma_f32 v[98:99], v[68:69], s[42:43], v[98:99] op_sel_hi:[1,0,1]
	v_pk_fma_f32 v[100:101], v[66:67], s[44:45], v[100:101] op_sel_hi:[1,0,1]
	v_pk_fma_f32 v[102:103], v[68:69], s[44:45], v[102:103] op_sel_hi:[1,0,1]
	v_pk_fma_f32 v[96:97], v[62:63], s[46:47], v[96:97] op_sel_hi:[1,0,1]
	v_pk_fma_f32 v[98:99], v[64:65], s[46:47], v[98:99] op_sel_hi:[1,0,1]
	v_pk_fma_f32 v[100:101], v[62:63], s[48:49], v[100:101] op_sel_hi:[1,0,1]
	v_pk_fma_f32 v[102:103], v[64:65], s[48:49], v[102:103] op_sel_hi:[1,0,1]
	v_pk_fma_f32 v[96:97], v[58:59], s[50:51], v[96:97] op_sel_hi:[1,0,1]
	v_pk_fma_f32 v[98:99], v[60:61], s[50:51], v[98:99] op_sel_hi:[1,0,1]
	v_pk_fma_f32 v[100:101], v[58:59], s[52:53], v[100:101] op_sel_hi:[1,0,1]
	v_pk_fma_f32 v[102:103], v[60:61], s[52:53], v[102:103] op_sel_hi:[1,0,1]
	v_pk_fma_f32 v[96:97], v[54:55], s[54:55], v[96:97] op_sel_hi:[1,0,1]
	v_pk_fma_f32 v[98:99], v[56:57], s[54:55], v[98:99] op_sel_hi:[1,0,1]
	v_pk_fma_f32 v[100:101], v[54:55], s[56:57], v[100:101] op_sel_hi:[1,0,1]
	v_pk_fma_f32 v[102:103], v[56:57], s[56:57], v[102:103] op_sel_hi:[1,0,1]
	v_pk_fma_f32 v[96:97], v[46:47], s[58:59], v[96:97] op_sel_hi:[1,0,1]
	v_pk_fma_f32 v[98:99], v[48:49], s[58:59], v[98:99] op_sel_hi:[1,0,1]
	v_pk_fma_f32 v[100:101], v[46:47], s[60:61], v[100:101] op_sel_hi:[1,0,1]
	v_pk_fma_f32 v[102:103], v[48:49], s[60:61], v[102:103] op_sel_hi:[1,0,1]
	v_pk_fma_f32 v[96:97], v[34:35], s[62:63], v[96:97] op_sel_hi:[1,0,1]
	v_pk_fma_f32 v[98:99], v[36:37], s[62:63], v[98:99] op_sel_hi:[1,0,1]
	v_pk_fma_f32 v[100:101], v[34:35], s[64:65], v[100:101] op_sel_hi:[1,0,1]
	v_pk_fma_f32 v[102:103], v[36:37], s[64:65], v[102:103] op_sel_hi:[1,0,1]
	v_pk_fma_f32 v[96:97], v[14:15], s[66:67], v[96:97] op_sel_hi:[1,0,1]
	v_pk_fma_f32 v[98:99], v[16:17], s[66:67], v[98:99] op_sel_hi:[1,0,1]
	v_pk_fma_f32 v[100:101], v[14:15], s[68:69], v[100:101] op_sel_hi:[1,0,1]
	v_pk_fma_f32 v[102:103], v[16:17], s[68:69], v[102:103] op_sel_hi:[1,0,1]
	s_cmp_lg_u32 s30, 8
	s_cbranch_scc1 .Lring_nostage
	v_lshlrev_b32_e32 v176, 4, v196
	v_lshl_add_u32 v176, v197, 14, v176
	s_mov_b32 m0, s33
	s_nop 0
	global_load_lds_dwordx4 v176, s[8:9]
	global_load_lds_dwordx4 v176, s[8:9] offset:1024
	global_load_lds_dwordx4 v176, s[8:9] offset:2048
	global_load_lds_dwordx4 v176, s[8:9] offset:3072
	v_add_u32_e32 v176, 0x1000, v176
	s_add_u32 s35, s33, 4096
	s_mov_b32 m0, s35
	s_nop 0
	global_load_lds_dwordx4 v176, s[8:9]
	global_load_lds_dwordx4 v176, s[8:9] offset:1024
	global_load_lds_dwordx4 v176, s[8:9] offset:2048
	global_load_lds_dwordx4 v176, s[8:9] offset:3072
	v_add_u32_e32 v176, 0x1000, v176
	s_add_u32 s35, s33, 8192
	s_mov_b32 m0, s35
	s_nop 0
	global_load_lds_dwordx4 v176, s[8:9]
	global_load_lds_dwordx4 v176, s[8:9] offset:1024
	global_load_lds_dwordx4 v176, s[8:9] offset:2048
.Lring_nostage:
	s_cmp_gt_u32 s30, 20
	s_cbranch_scc1 .Lring_noload_0
	global_load_dword v107, v[118:119], off nt
	global_load_dwordx4 v[70:73], v[116:117], off nt
	global_load_dwordx4 v[66:69], v[116:117], off offset:512 nt
	global_load_dwordx4 v[62:65], v[116:117], off offset:1024 nt
	global_load_dwordx4 v[58:61], v[116:117], off offset:1536 nt
	global_load_dwordx4 v[54:57], v[116:117], off offset:2048 nt
	global_load_dwordx4 v[46:49], v[116:117], off offset:2560 nt
	global_load_dwordx4 v[34:37], v[116:117], off offset:3072 nt
	global_load_dwordx4 v[14:17], v[116:117], off offset:3584 nt
	v_lshl_add_u64 v[116:117], v[116:117], 0, s[16:17]
	v_lshl_add_u64 v[118:119], v[118:119], 0, 32

.Lring_done:
	s_setprio 0
	v_mov_b32_e32 v240, v96
	v_mov_b32_e32 v241, v97
	v_mov_b32_e32 v242, v98
	v_mov_b32_e32 v243, v99
	v_mov_b32_e32 v244, v100
	v_mov_b32_e32 v245, v101
	v_mov_b32_e32 v246, v102
	v_mov_b32_e32 v247, v103
	v_mov_b32_e32 v248, v104
	v_mov_b32_e32 v249, v105
	s_movk_i32 s0, 0x640
	v_mov_b32_e32 v14, 0x8200
	v_mad_u32_u24 v205, v197, s0, v14
	v_lshlrev_b32_e32 v10, 4, v106
	v_or_b32_e32 v6, 0x2000, v196
	v_add_lshl_u32 v7, v122, v6, 4
	v_lshlrev_b32_e32 v11, 4, v196
	v_add_u32_e32 v11, s33, v11
	ds_read_b128 v[158:161], v11
	ds_read_b128 v[154:157], v11 offset:1024
	ds_read_b128 v[146:149], v11 offset:2048
	ds_read_b128 v[138:141], v11 offset:3072
	ds_read_b128 v[118:121], v11 offset:4096
	ds_read_b128 v[106:109], v11 offset:5120
	ds_read_b128 v[98:101], v11 offset:6144
	ds_read_b128 v[102:105], v11 offset:7168
	ds_read_b128 v[170:173], v11 offset:8192
	ds_read_b128 v[166:169], v11 offset:9216
	ds_read_b128 v[178:181], v11 offset:10240
	global_load_dwordx4 v[174:177], v142, s[8:9]
	global_load_dwordx4 v[162:165], v143, s[8:9]
	s_nop 0
	global_load_dwordx4 v[134:137], v144, s[8:9]
	global_load_dwordx4 v[114:117], v145, s[8:9]
	global_load_dwordx4 v[110:113], v150, s[8:9]
	global_load_dwordx4 v[94:97], v7, s[8:9]
	global_load_dwordx4 v[90:93], v7, s[8:9] offset:1024
	global_load_dwordx4 v[78:81], v7, s[8:9] offset:2048
	global_load_dwordx4 v[74:77], v7, s[8:9] offset:3072
	v_add_lshl_u32 v7, v123, v6, 4
	v_add_lshl_u32 v8, v124, v6, 4
	global_load_dwordx4 v[66:69], v7, s[8:9]
	global_load_dwordx4 v[58:61], v8, s[8:9]
	v_add_lshl_u32 v7, v125, v6, 4
	v_add_lshl_u32 v8, v126, v6, 4
	global_load_dwordx4 v[62:65], v7, s[8:9]
	global_load_dwordx4 v[54:57], v8, s[8:9]
	v_add_lshl_u32 v7, v127, v6, 4
	v_add_lshl_u32 v8, v128, v6, 4
	global_load_dwordx4 v[150:153], v7, s[8:9]
	global_load_dwordx4 v[142:145], v8, s[8:9]
	v_add_lshl_u32 v7, v129, v6, 4
	v_add_lshl_u32 v8, v130, v6, 4
	global_load_dwordx4 v[130:133], v7, s[8:9]
	global_load_dwordx4 v[126:129], v8, s[8:9]
	v_add_lshl_u32 v7, v192, v6, 4
	v_add_lshl_u32 v8, v202, v6, 4
	global_load_dwordx4 v[122:125], v7, s[8:9]
	global_load_dwordx4 v[82:85], v8, s[8:9]
	v_add_lshl_u32 v7, v203, v6, 4
	v_add_lshl_u32 v6, v204, v6, 4
	global_load_dwordx4 v[86:89], v7, s[8:9]
	global_load_dwordx4 v[70:73], v6, s[8:9]
	v_lshlrev_b32_e32 v187, 2, v195
	v_and_or_b32 v190, v187, 4, s31
	v_or_b32_e32 v208, 1, v190
	v_mul_u32_u24_e32 v6, 0x300, v197
	v_ashrrev_i32_e32 v191, 31, v190
	v_ashrrev_i32_e32 v209, 31, v208
	v_or_b32_e32 v6, v196, v6
	v_lshlrev_b64 v[210:211], 9, v[190:191]
	v_lshlrev_b32_e32 v191, 2, v1
	v_lshlrev_b64 v[222:223], 9, v[208:209]
	v_or_b32_e32 v208, 2, v190
	v_mov_b32_e32 v193, 0
	v_lshlrev_b32_e32 v14, 4, v6
	v_lshl_or_b32 v192, v197, 7, v191
	s_movk_i32 s2, 0xfe00
	v_ashrrev_i32_e32 v209, 31, v208
	v_or_b32_e32 v6, 0x40000, v14
	s_movk_i32 s1, 0x100
	v_lshl_add_u64 v[220:221], s[22:23], 0, v[192:193]
	s_mov_b32 s3, -1
	v_lshlrev_b64 v[226:227], 9, v[208:209]
	v_or_b32_e32 v208, 3, v190
	global_load_dwordx4 v[50:53], v6, s[8:9]
	global_load_dwordx4 v[46:49], v6, s[8:9] offset:1024
	global_load_dwordx4 v[42:45], v6, s[8:9] offset:2048
	global_load_dwordx4 v[30:33], v6, s[8:9] offset:3072
	v_add_u32_e32 v6, 0x41000, v14
	v_add_u32_e32 v7, 0x41400, v14
	v_lshl_add_u64 v[212:213], s[20:21], 0, v[192:193]
	v_lshl_add_u64 v[202:203], v[220:221], 0, s[2:3]
	v_cmp_gt_u32_e32 vcc, s1, v0
	v_ashrrev_i32_e32 v209, 31, v208
	s_movk_i32 s2, 0xfe40
	global_load_dwordx4 v[38:41], v6, s[8:9]
	global_load_dwordx4 v[22:25], v7, s[8:9]
	v_add_u32_e32 v6, 0x41800, v14
	v_add_u32_e32 v7, 0x41c00, v14
	v_cndmask_b32_e32 v203, v203, v213, vcc
	v_cndmask_b32_e32 v202, v202, v212, vcc
	v_lshlrev_b64 v[230:231], 9, v[208:209]
	s_mov_b32 s3, -1
	global_load_dwordx4 v[34:37], v6, s[8:9]
	global_load_dwordx4 v[10:13], v7, s[8:9]
	v_add_u32_e32 v6, 0x42000, v14
	v_add_u32_e32 v7, 0x42400, v14
	v_add_u32_e32 v15, 0x42800, v14
	v_add_u32_e32 v18, 0x42c00, v14
	v_lshl_add_u64 v[206:207], v[202:203], 0, v[210:211]
	v_lshl_add_u64 v[224:225], v[202:203], 0, v[222:223]
	v_lshl_add_u64 v[228:229], v[202:203], 0, v[226:227]
	v_lshl_add_u64 v[202:203], v[202:203], 0, v[230:231]
	v_lshl_add_u64 v[212:213], v[212:213], 0, 64
	v_lshl_add_u64 v[220:221], v[220:221], 0, s[2:3]
	global_load_dwordx4 v[26:29], v6, s[8:9]
	s_nop 0
	global_load_dwordx4 v[6:9], v7, s[8:9]
	s_nop 0
	global_load_dwordx4 v[14:17], v15, s[8:9]
	s_nop 0
	global_load_dwordx4 v[18:21], v18, s[8:9]
	s_nop 0
	global_load_dword v208, v[206:207], off
	s_nop 0
	global_load_dword v207, v[224:225], off
	global_load_dword v204, v[228:229], off
	s_nop 0
	global_load_dword v203, v[202:203], off
	s_nop 0
	global_load_dword v206, v192, s[10:11]
	global_load_dword v202, v192, s[10:11] offset:64
	v_cndmask_b32_e32 v213, v221, v213, vcc
	v_cndmask_b32_e32 v212, v220, v212, vcc
	v_lshl_add_u64 v[210:211], v[212:213], 0, v[210:211]
	v_lshl_add_u64 v[220:221], v[212:213], 0, v[222:223]
	v_lshl_add_u64 v[222:223], v[212:213], 0, v[226:227]
	v_lshl_add_u64 v[224:225], v[212:213], 0, v[230:231]
	global_load_dword v212, v[210:211], off
	s_nop 0
	global_load_dword v211, v[220:221], off
	global_load_dword v210, v[222:223], off
	global_load_dword v209, v[224:225], off
	v_lshl_or_b32 v190, v197, 4, v1
	v_lshlrev_b32_e32 v186, 2, v190
	global_load_dword v189, v186, s[24:25]
	global_load_dword v188, v186, s[26:27]
	v_mov_b32_e32 v233, v249
	v_mov_b32_e32 v232, v248
	v_mov_b32_e32 v214, v240
	v_mov_b32_e32 v215, v241
	v_mov_b32_e32 v216, v242
	v_mov_b32_e32 v217, v243
	v_mov_b32_e32 v218, v244
	v_mov_b32_e32 v219, v245
	v_mov_b32_e32 v220, v246
	v_mov_b32_e32 v221, v247
	s_nop 1
	v_add_f32_dpp v2, v233, v233 row_ror:8 row_mask:0xf bank_mask:0xf bound_ctrl:1
	v_mov_b32_e32 v3, v2
	s_nop 1
	v_permlane16_swap_b32_e32 v2, v3
	v_add_f32_e32 v2, v2, v3
	v_mov_b32_e32 v3, v2
	s_nop 1
	v_permlane32_swap_b32_e32 v2, v3
	v_add_f32_e32 v2, v2, v3
	v_readlane_b32 s2, v232, 4
	v_readlane_b32 s4, v2, 4
	v_readlane_b32 s5, v2, 0
	v_readlane_b32 s3, v232, 0
	v_div_scale_f32 v3, s[0:1], s4, s4, 1.0
	v_rcp_f32_e32 v4, v3
	v_lshl_add_u64 v[182:183], v[182:183], 2, s[28:29]
	v_fma_f32 v2, -v3, v4, 1.0
	v_fmac_f32_e32 v4, v2, v4
	v_div_scale_f32 v2, vcc, 1.0, s4, 1.0
	v_mul_f32_e32 v5, v2, v4
	v_fma_f32 v192, -v3, v5, v2
	v_fmac_f32_e32 v5, v192, v4
	v_fma_f32 v2, -v3, v5, v2
	v_div_scale_f32 v3, s[0:1], s5, s5, 1.0
	v_rcp_f32_e32 v192, v3
	v_div_fmas_f32 v2, v2, v4, v5
	v_div_fixup_f32 v2, v2, s4, 1.0
	s_movk_i32 s0, 0xc8
	v_fma_f32 v4, -v3, v192, 1.0
	v_fmac_f32_e32 v192, v4, v192
	v_div_scale_f32 v4, vcc, 1.0, s5, 1.0
	v_mul_f32_e32 v5, v4, v192
	v_fma_f32 v213, -v3, v5, v4
	v_fmac_f32_e32 v5, v213, v192
	v_fma_f32 v3, -v3, v5, v4
	v_div_fmas_f32 v3, v3, v192, v5
	v_div_fixup_f32 v4, v3, s5, 1.0
	v_pk_mul_f32 v[216:217], v[216:217], v[4:5] op_sel_hi:[1,0]
	v_pk_mul_f32 v[214:215], v[214:215], v[4:5] op_sel_hi:[1,0]
	v_cvt_pk_f16_f32 v217, v216, v217
	v_cvt_pk_f16_f32 v216, v214, v215
	v_pk_mul_f32 v[214:215], v[220:221], v[2:3] op_sel_hi:[1,0]
	v_pk_mul_f32 v[218:219], v[218:219], v[2:3] op_sel_hi:[1,0]
	v_add_u32_e32 v3, v205, v184
	ds_read2_b32 v[220:221], v3 offset0:128 offset1:200
	v_cvt_pk_f16_f32 v215, v214, v215
	v_cvt_pk_f16_f32 v214, v218, v219
	ds_read2st64_b32 v[218:219], v3 offset1:1
	v_add_u32_e32 v192, 32, v3
	ds_write2st64_b64 v185, v[216:217], v[214:215] offset1:1
	ds_read2st64_b32 v[214:215], v192 offset0:4 offset1:5
	s_waitcnt lgkmcnt(3)
	v_subrev_f32_e32 v5, s2, v221
	v_exp_f32_e32 v5, v5
	s_waitcnt lgkmcnt(2)
	v_subrev_f32_e32 v185, s3, v218
	v_exp_f32_e32 v185, v185
	s_waitcnt lgkmcnt(0)
	v_subrev_f32_e32 v205, s2, v214
	v_mul_f32_e32 v5, v2, v5
	v_subrev_f32_e32 v192, s3, v219
	v_exp_f32_e32 v205, v205
	v_fmac_f32_e32 v5, v4, v185
	v_mov_b32_e32 v185, v193
	v_exp_f32_e32 v192, v192
	v_lshl_add_u64 v[182:183], v[182:183], 0, v[184:185]
	v_subrev_f32_e32 v185, s2, v215
	v_mul_f32_e32 v5, 0.5, v5
	v_subrev_f32_e32 v184, s3, v220
	v_exp_f32_e32 v185, v185
	global_store_dword v[182:183], v5, off
	v_mul_f32_e32 v5, v2, v205
	v_exp_f32_e32 v184, v184
	v_fmac_f32_e32 v5, v4, v192
	v_mul_f32_e32 v5, 0.5, v5
	global_store_dword v[182:183], v5, off offset:256
	v_mul_f32_e32 v5, v2, v185
	v_fmac_f32_e32 v5, v4, v184
	v_mul_f32_e32 v5, 0.5, v5
	global_store_dword v[182:183], v5, off offset:512
	v_or_b32_e32 v5, 0xc0, v196
	v_cmp_gt_u32_e32 vcc, s0, v5
	s_and_saveexec_b64 s[0:1], vcc
	s_cbranch_execz .LBB1_19
	v_add_u32_e32 v3, 0x300, v3
	ds_read2_b32 v[184:185], v3 offset1:200
	s_waitcnt lgkmcnt(0)
	v_subrev_f32_e32 v3, s3, v184
	v_subrev_f32_e32 v5, s2, v185
	v_exp_f32_e32 v184, v3
	v_exp_f32_e32 v185, v5
	v_mov_b32_e32 v5, v2
	v_pk_mul_f32 v[2:3], v[4:5], v[184:185]
	s_nop 0
	v_add_f32_e32 v2, v2, v3
	v_mul_f32_e32 v2, 0.5, v2
	global_store_dword v[182:183], v2, off offset:768

	.amdhsa_kernel _Z10k_attn_epiILi2EEvPKfS1_PKiPKDF16_S5_PfS1_S1_S5_S1_S1_S1_S1_S1_S6_
		.amdhsa_group_segment_fixed_size 161536
		.amdhsa_private_segment_fixed_size 0
		.amdhsa_kernarg_size 120
		.amdhsa_user_sgpr_count 2
		.amdhsa_user_sgpr_dispatch_ptr 0
		.amdhsa_user_sgpr_queue_ptr 0
		.amdhsa_user_sgpr_kernarg_segment_ptr 1
		.amdhsa_user_sgpr_dispatch_id 0
		.amdhsa_user_sgpr_kernarg_preload_length 0
		.amdhsa_user_sgpr_kernarg_preload_offset 0
		.amdhsa_user_sgpr_private_segment_size 0
		.amdhsa_uses_dynamic_stack 0
		.amdhsa_enable_private_segment 0
		.amdhsa_system_sgpr_workgroup_id_x 1
		.amdhsa_system_sgpr_workgroup_id_y 0
		.amdhsa_system_sgpr_workgroup_id_z 0
		.amdhsa_system_sgpr_workgroup_info 0
		.amdhsa_system_vgpr_workitem_id 0
		.amdhsa_next_free_vgpr 256
		.amdhsa_next_free_sgpr 96
		.amdhsa_accum_offset 256
		.amdhsa_reserve_vcc 1
		.amdhsa_float_round_mode_32 0
		.amdhsa_float_round_mode_16_64 0
		.amdhsa_float_denorm_mode_32 3
		.amdhsa_float_denorm_mode_16_64 3
		.amdhsa_dx10_clamp 1
		.amdhsa_ieee_mode 1
		.amdhsa_fp16_overflow 0
		.amdhsa_tg_split 0
		.amdhsa_exception_fp_ieee_invalid_op 0
		.amdhsa_exception_fp_denorm_src 0
		.amdhsa_exception_fp_ieee_div_zero 0
		.amdhsa_exception_fp_ieee_overflow 0
		.amdhsa_exception_fp_ieee_underflow 0
		.amdhsa_exception_fp_ieee_inexact 0
		.amdhsa_exception_int_div_zero 0
	.end_amdhsa_kernel

amdhsa.kernels:
  - .agpr_count:     0
    .args:
      - .actual_access:  read_only
        .address_space:  global
        .offset:         0
        .size:           8
        .value_kind:     global_buffer
      - .actual_access:  read_only
        .address_space:  global
        .offset:         8
        .size:           8
        .value_kind:     global_buffer
      - .actual_access:  read_only
        .address_space:  global
        .offset:         16
        .size:           8
        .value_kind:     global_buffer
      - .actual_access:  read_only
        .address_space:  global
        .offset:         24
        .size:           8
        .value_kind:     global_buffer
      - .actual_access:  read_only
        .address_space:  global
        .offset:         32
        .size:           8
        .value_kind:     global_buffer
      - .actual_access:  read_only
        .address_space:  global
        .offset:         40
        .size:           8
        .value_kind:     global_buffer
      - .actual_access:  write_only
        .address_space:  global
        .offset:         48
        .size:           8
        .value_kind:     global_buffer
      - .actual_access:  write_only
        .address_space:  global
        .offset:         56
        .size:           8
        .value_kind:     global_buffer
      - .actual_access:  write_only
        .address_space:  global
        .offset:         64
        .size:           8
        .value_kind:     global_buffer
    .group_segment_fixed_size: 0
    .kernarg_segment_align: 8
    .kernarg_segment_size: 72
    .language:       OpenCL C
    .language_version:
      - 2
      - 0
    .max_flat_workgroup_size: 320
    .name:           _Z6k_prepPKfS0_S0_S0_S0_S0_PDF16_S1_S1_
    .private_segment_fixed_size: 0
    .sgpr_count:     20
    .sgpr_spill_count: 0
    .symbol:         _Z6k_prepPKfS0_S0_S0_S0_S0_PDF16_S1_S1_.kd
    .uniform_work_group_size: 1
    .uses_dynamic_stack: false
    .vgpr_count:     16
    .vgpr_spill_count: 0
    .wavefront_size: 64
  - .agpr_count:     0
    .args:
      - .actual_access:  read_only
        .address_space:  global
        .offset:         0
        .size:           8
        .value_kind:     global_buffer
      - .actual_access:  read_only
        .address_space:  global
        .offset:         8
        .size:           8
        .value_kind:     global_buffer
      - .actual_access:  read_only
        .address_space:  global
        .offset:         16
        .size:           8
        .value_kind:     global_buffer
      - .actual_access:  read_only
        .address_space:  global
        .offset:         24
        .size:           8
        .value_kind:     global_buffer
      - .actual_access:  read_only
        .address_space:  global
        .offset:         32
        .size:           8
        .value_kind:     global_buffer
      - .actual_access:  write_only
        .address_space:  global
        .offset:         40
        .size:           8
        .value_kind:     global_buffer
      - .actual_access:  read_only
        .address_space:  global
        .offset:         48
        .size:           8
        .value_kind:     global_buffer
      - .actual_access:  read_only
        .address_space:  global
        .offset:         56
        .size:           8
        .value_kind:     global_buffer
      - .actual_access:  read_only
        .address_space:  global
        .offset:         64
        .size:           8
        .value_kind:     global_buffer
      - .actual_access:  read_only
        .address_space:  global
        .offset:         72
        .size:           8
        .value_kind:     global_buffer
      - .actual_access:  read_only
        .address_space:  global
        .offset:         80
        .size:           8
        .value_kind:     global_buffer
      - .actual_access:  read_only
        .address_space:  global
        .offset:         88
        .size:           8
        .value_kind:     global_buffer
      - .actual_access:  read_only
        .address_space:  global
        .offset:         96
        .size:           8
        .value_kind:     global_buffer
      - .actual_access:  read_only
        .address_space:  global
        .offset:         104
        .size:           8
        .value_kind:     global_buffer
      - .actual_access:  write_only
        .address_space:  global
        .offset:         112
        .size:           8
        .value_kind:     global_buffer
    .group_segment_fixed_size: 161536
    .kernarg_segment_align: 8
    .kernarg_segment_size: 120
    .language:       OpenCL C
    .language_version:
      - 2
      - 0
    .max_flat_workgroup_size: 512
    .name:           _Z10k_attn_epiILi2EEvPKfS1_PKiPKDF16_S5_PfS1_S1_S5_S1_S1_S1_S1_S1_S6_
    .private_segment_fixed_size: 0
    .sgpr_count:     76
    .sgpr_spill_count: 0
    .symbol:         _Z10k_attn_epiILi2EEvPKfS1_PKiPKDF16_S5_PfS1_S1_S5_S1_S1_S1_S1_S1_S6_.kd
    .uniform_work_group_size: 1
    .uses_dynamic_stack: false
    .vgpr_count:     256
    .vgpr_spill_count: 0
    .wavefront_size: 64
